# grid barrier: every workgroup polls the arrival counter TOP against (generation+1)*nx; the last leader's returning-atomic round trip and the TOPGEN bump leave the release path
# speedup vs baseline: 1.0006x; 1.0006x over previous
; __device__ __forceinline__ unsigned xb_ld(unsigned* p)              { return __hip_atomic_load(p, __ATOMIC_RELAXED, __HIP_MEMORY_SCOPE_AGENT); }
; __device__ __forceinline__ unsigned xb_add(unsigned* p, unsigned v) { return __hip_atomic_fetch_add(p, v, __ATOMIC_RELAXED, __HIP_MEMORY_SCOPE_AGENT); }
; #define XB_SPIN(cond, bar) do { unsigned _sp = 0; while (cond) { __builtin_amdgcn_s_sleep(1); \
;     if ((++_sp & 255u) == 0u) { if (xb_ld(&(bar)[XB_TMO])) break; if (_sp > XB_SPIN_CAP) { atomicAdd(&(bar)[XB_TMO], 1u); break; } } } } while (0)
; __device__ __forceinline__ void xcd_barrier(const XcdBarrier& b) {
;     ...
;         const unsigned old = xb_add(&bar[XB_XSUB(b.x)], 1u);
;         const unsigned gen = old / nloc;
;         if (old + 1u == (gen + 1u) * nloc) {
;             __builtin_amdgcn_fence(__ATOMIC_RELEASE, "agent");
;             asm volatile("s_waitcnt vmcnt(0)" ::: "memory");
;             const unsigned og = xb_add(&bar[XB_TOP], 1u);
;             const unsigned tg = og / nx;
;             if (og + 1u == (tg + 1u) * nx) xb_add(&bar[XB_TOPGEN], 1u);
;             else XB_SPIN(xb_ld(&bar[XB_TOPGEN]) == tg, bar);
;             __builtin_amdgcn_fence(__ATOMIC_ACQUIRE, "agent");
;             xb_add(&bar[XB_XGEN(b.x)], 1u);
;             asm volatile("s_waitcnt vmcnt(0)" ::: "memory");
;         } else {
;             XB_SPIN(xb_ld(&bar[XB_XGEN(b.x)]) == gen, bar);
.LBB0_40:
	s_lshl_b32 s3, s82, 8
	s_add_u32 s6, s80, s3
	s_addc_u32 s7, s81, 0
	v_mov_b32_e32 v2, 0x1000
	v_mov_b32_e32 v4, 1
	global_atomic_add v4, v2, v4, s[6:7] offset:1024 sc0
	v_cvt_f32_u32_e32 v2, v3
	v_sub_u32_e32 v5, 0, v3
	v_rcp_iflag_f32_e32 v2, v2
	s_nop 0
	v_mul_f32_e32 v2, 0x4f7ffffe, v2
	v_cvt_u32_f32_e32 v2, v2
	v_mul_lo_u32 v5, v5, v2
	v_mul_hi_u32 v5, v2, v5
	v_add_u32_e32 v2, v2, v5
	s_waitcnt vmcnt(0)
	v_mul_hi_u32 v2, v4, v2
	v_mul_lo_u32 v5, v2, v3
	v_sub_u32_e32 v5, v4, v5
	v_add_u32_e32 v6, 1, v2
	v_cmp_ge_u32_e32 vcc, v5, v3
	v_add_u32_e32 v4, 1, v4
	s_nop 0
	v_cndmask_b32_e32 v2, v2, v6, vcc
	v_sub_u32_e32 v6, v5, v3
	v_cndmask_b32_e32 v5, v5, v6, vcc
	v_add_u32_e32 v6, 1, v2
	v_cmp_ge_u32_e32 vcc, v5, v3
	s_nop 1
	v_cndmask_b32_e32 v2, v2, v6, vcc
	v_mul_lo_u32 v5, v3, v2
	v_add_u32_e32 v3, v5, v3
	v_cmp_ne_u32_e32 vcc, v4, v3
	s_and_saveexec_b64 s[8:9], vcc
	s_xor_b64 s[8:9], exec, s[8:9]
	s_cbranch_execz .LBB0_54
	s_waitcnt lgkmcnt(0)
	v_add_u32_e32 v19, 1, v2
	v_mul_lo_u32 v19, v19, v1
	v_mov_b32_e32 v1, 0x7000
	global_load_dword v1, v1, s[90:91] offset:1024 sc1
	s_add_u32 s14, s90, 0x7400
	s_addc_u32 s15, s91, 0
	s_waitcnt vmcnt(0)
	v_cmp_lt_u32_e32 vcc, v1, v19
	s_and_saveexec_b64 s[10:11], vcc
	s_cbranch_execz .LBB0_53
	s_add_u32 s12, s90, 0x4200
	s_addc_u32 s13, s91, 0
	s_mov_b32 s3, 1
	s_mov_b64 s[26:27], 0
	v_mov_b32_e32 v1, 0
	s_branch .LBB0_44

; __device__ __forceinline__ unsigned xb_ld(unsigned* p)              { return __hip_atomic_load(p, __ATOMIC_RELAXED, __HIP_MEMORY_SCOPE_AGENT); }
; #define XB_SPIN(cond, bar) do { unsigned _sp = 0; while (cond) { __builtin_amdgcn_s_sleep(1); \
;     if ((++_sp & 255u) == 0u) { if (xb_ld(&(bar)[XB_TMO])) break; if (_sp > XB_SPIN_CAP) { atomicAdd(&(bar)[XB_TMO], 1u); break; } } } } while (0)
; __device__ __forceinline__ void xcd_barrier(const XcdBarrier& b) {
;     ...
;             XB_SPIN(xb_ld(&bar[XB_XGEN(b.x)]) == gen, bar);
.LBB0_48:
	global_load_dword v3, v1, s[14:15] sc1
	s_add_i32 s3, s3, 1
	s_mov_b64 s[40:41], -1
	s_waitcnt vmcnt(0)
	v_cmp_ge_u32_e32 vcc, v3, v19
	s_orn2_b64 s[38:39], vcc, exec
	s_branch .LBB0_43

; __device__ __forceinline__ unsigned xb_ld(unsigned* p)              { return __hip_atomic_load(p, __ATOMIC_RELAXED, __HIP_MEMORY_SCOPE_AGENT); }
; __device__ __forceinline__ unsigned xb_add(unsigned* p, unsigned v) { return __hip_atomic_fetch_add(p, v, __ATOMIC_RELAXED, __HIP_MEMORY_SCOPE_AGENT); }
; #define XB_SPIN(cond, bar) do { unsigned _sp = 0; while (cond) { __builtin_amdgcn_s_sleep(1); \
;     if ((++_sp & 255u) == 0u) { if (xb_ld(&(bar)[XB_TMO])) break; if (_sp > XB_SPIN_CAP) { atomicAdd(&(bar)[XB_TMO], 1u); break; } } } } while (0)
; __device__ __forceinline__ void xcd_barrier(const XcdBarrier& b) {
;     ...
;         if (old + 1u == (gen + 1u) * nloc) {
;             __builtin_amdgcn_fence(__ATOMIC_RELEASE, "agent");
;             asm volatile("s_waitcnt vmcnt(0)" ::: "memory");
;             const unsigned og = xb_add(&bar[XB_TOP], 1u);
;             const unsigned tg = og / nx;
;             if (og + 1u == (tg + 1u) * nx) xb_add(&bar[XB_TOPGEN], 1u);
;             else XB_SPIN(xb_ld(&bar[XB_TOPGEN]) == tg, bar);
.LBB0_54:
	s_andn2_saveexec_b64 s[8:9], s[8:9]
	s_cbranch_execz .LBB0_72
	s_mov_b64 s[8:9], exec
	v_add_u32_e32 v19, 1, v2
	v_mul_lo_u32 v19, v19, v1
	buffer_wbl2 sc1
	s_waitcnt lgkmcnt(0)
	s_waitcnt vmcnt(0)
	v_mbcnt_lo_u32_b32 v2, s8, 0
	v_mbcnt_hi_u32_b32 v2, s9, v2
	v_cmp_eq_u32_e32 vcc, 0, v2
	s_and_saveexec_b64 s[10:11], vcc
	s_cbranch_execz .LBB0_57
	s_bcnt1_i32_b64 s3, s[8:9]
	v_mov_b32_e32 v3, 0x7000
	v_mov_b32_e32 v4, s3
	global_atomic_add v3, v3, v4, s[90:91] offset:1024 sc0
.LBB0_57:
	s_or_b64 exec, exec, s[10:11]
	v_cvt_f32_u32_e32 v4, v1
	s_waitcnt vmcnt(0)
	v_readfirstlane_b32 s3, v3
	s_add_u32 s10, s90, 0x7400
	s_addc_u32 s11, s91, 0
	v_rcp_iflag_f32_e32 v4, v4
	v_add_u32_e32 v2, s3, v2
	v_add_u32_e32 v5, 1, v2
	s_mov_b64 s[12:13], -1
	v_mul_f32_e32 v3, 0x4f7ffffe, v4
	v_cvt_u32_f32_e32 v3, v3
	v_sub_u32_e32 v4, 0, v1
	v_mul_lo_u32 v4, v4, v3
	v_mul_hi_u32 v4, v3, v4
	v_add_u32_e32 v3, v3, v4
	v_mul_hi_u32 v3, v2, v3
	v_mul_lo_u32 v4, v3, v1
	v_sub_u32_e32 v2, v2, v4
	v_add_u32_e32 v6, 1, v3
	v_cmp_ge_u32_e32 vcc, v2, v1
	v_sub_u32_e32 v4, v2, v1
	s_nop 0
	v_cndmask_b32_e32 v3, v3, v6, vcc
	v_cndmask_b32_e32 v2, v2, v4, vcc
	v_add_u32_e32 v4, 1, v3
	v_cmp_ge_u32_e32 vcc, v2, v1
	s_nop 1
	v_cndmask_b32_e32 v4, v3, v4, vcc
	v_mul_lo_u32 v2, v1, v4
	v_add_u32_e32 v1, v2, v1
	v_cmp_ne_u32_e32 vcc, v5, v1
	v_mov_b64_e32 v[2:3], s[10:11]
	s_and_saveexec_b64 s[8:9], vcc
	s_cbranch_execz .LBB0_69
	v_mov_b32_e32 v1, 0
	global_load_dword v2, v1, s[10:11] sc1
	s_mov_b64 s[26:27], 0
	s_waitcnt vmcnt(0)
	v_cmp_lt_u32_e32 vcc, v2, v19
	s_and_saveexec_b64 s[14:15], vcc
	s_cbranch_execz .LBB0_68
	s_add_u32 s12, s90, 0x4200
	s_addc_u32 s13, s91, 0
	s_mov_b32 s3, 1
	s_branch .LBB0_61

; __device__ __forceinline__ unsigned xb_ld(unsigned* p)              { return __hip_atomic_load(p, __ATOMIC_RELAXED, __HIP_MEMORY_SCOPE_AGENT); }
; #define XB_SPIN(cond, bar) do { unsigned _sp = 0; while (cond) { __builtin_amdgcn_s_sleep(1); \
;     if ((++_sp & 255u) == 0u) { if (xb_ld(&(bar)[XB_TMO])) break; if (_sp > XB_SPIN_CAP) { atomicAdd(&(bar)[XB_TMO], 1u); break; } } } } while (0)
; __device__ __forceinline__ void xcd_barrier(const XcdBarrier& b) {
;     ...
;             else XB_SPIN(xb_ld(&bar[XB_TOPGEN]) == tg, bar);
.LBB0_65:
	global_load_dword v2, v1, s[10:11] sc1
	s_add_i32 s3, s3, 1
	s_mov_b64 s[38:39], -1
	s_waitcnt vmcnt(0)
	v_cmp_ge_u32_e32 vcc, v2, v19
	s_orn2_b64 s[42:43], vcc, exec
	s_branch .LBB0_60

; __device__ __forceinline__ unsigned xb_ld(unsigned* p)              { return __hip_atomic_load(p, __ATOMIC_RELAXED, __HIP_MEMORY_SCOPE_AGENT); }
; __device__ __forceinline__ unsigned xb_add(unsigned* p, unsigned v) { return __hip_atomic_fetch_add(p, v, __ATOMIC_RELAXED, __HIP_MEMORY_SCOPE_AGENT); }
; #define XB_SPIN(cond, bar) do { unsigned _sp = 0; while (cond) { __builtin_amdgcn_s_sleep(1); \
;     if ((++_sp & 255u) == 0u) { if (xb_ld(&(bar)[XB_TMO])) break; if (_sp > XB_SPIN_CAP) { atomicAdd(&(bar)[XB_TMO], 1u); break; } } } } while (0)
; __device__ __forceinline__ void xcd_barrier(const XcdBarrier& b) {
;     ...
;             if (og + 1u == (tg + 1u) * nx) xb_add(&bar[XB_TOPGEN], 1u);
;             else XB_SPIN(xb_ld(&bar[XB_TOPGEN]) == tg, bar);
;             __builtin_amdgcn_fence(__ATOMIC_ACQUIRE, "agent");
;             xb_add(&bar[XB_XGEN(b.x)], 1u);
;             asm volatile("s_waitcnt vmcnt(0)" ::: "memory");
;         } else {
;             XB_SPIN(xb_ld(&bar[XB_XGEN(b.x)]) == gen, bar);
;             __builtin_amdgcn_fence(__ATOMIC_ACQUIRE, "agent");
;             asm volatile("s_waitcnt vmcnt(0)" ::: "memory");
.LBB0_69:
	s_or_b64 exec, exec, s[8:9]
	s_and_saveexec_b64 s[8:9], s[12:13]
	s_cbranch_execz .LBB0_71
	v_mov_b32_e32 v1, 1
.LBB0_71:
	s_or_b64 exec, exec, s[8:9]
	v_mov_b32_e32 v1, 0x2000
	v_mov_b32_e32 v2, 1
	s_waitcnt vmcnt(0)
	buffer_inv sc1
	s_waitcnt vmcnt(0)

; __device__ __forceinline__ unsigned xb_ld(unsigned* p)              { return __hip_atomic_load(p, __ATOMIC_RELAXED, __HIP_MEMORY_SCOPE_AGENT); }
; __device__ __forceinline__ unsigned xb_add(unsigned* p, unsigned v) { return __hip_atomic_fetch_add(p, v, __ATOMIC_RELAXED, __HIP_MEMORY_SCOPE_AGENT); }
; #define XB_SPIN(cond, bar) do { unsigned _sp = 0; while (cond) { __builtin_amdgcn_s_sleep(1); \
;     if ((++_sp & 255u) == 0u) { if (xb_ld(&(bar)[XB_TMO])) break; if (_sp > XB_SPIN_CAP) { atomicAdd(&(bar)[XB_TMO], 1u); break; } } } } while (0)
; __device__ __forceinline__ void xcd_barrier(const XcdBarrier& b) {
;     ...
;         const unsigned old = xb_add(&bar[XB_XSUB(b.x)], 1u);
;         const unsigned gen = old / nloc;
;         if (old + 1u == (gen + 1u) * nloc) {
;             __builtin_amdgcn_fence(__ATOMIC_RELEASE, "agent");
;             asm volatile("s_waitcnt vmcnt(0)" ::: "memory");
;             const unsigned og = xb_add(&bar[XB_TOP], 1u);
;             const unsigned tg = og / nx;
;             if (og + 1u == (tg + 1u) * nx) xb_add(&bar[XB_TOPGEN], 1u);
;             else XB_SPIN(xb_ld(&bar[XB_TOPGEN]) == tg, bar);
;             __builtin_amdgcn_fence(__ATOMIC_ACQUIRE, "agent");
;             xb_add(&bar[XB_XGEN(b.x)], 1u);
;             asm volatile("s_waitcnt vmcnt(0)" ::: "memory");
;         } else {
;             XB_SPIN(xb_ld(&bar[XB_XGEN(b.x)]) == gen, bar);
.LBB0_168:
	s_lshl_b32 s3, s82, 8
	s_add_u32 s4, s80, s3
	s_addc_u32 s5, s81, 0
	v_mov_b32_e32 v2, 0x1000
	v_mov_b32_e32 v4, 1
	global_atomic_add v4, v2, v4, s[4:5] offset:1024 sc0
	v_cvt_f32_u32_e32 v2, v3
	v_sub_u32_e32 v5, 0, v3
	v_rcp_iflag_f32_e32 v2, v2
	s_nop 0
	v_mul_f32_e32 v2, 0x4f7ffffe, v2
	v_cvt_u32_f32_e32 v2, v2
	v_mul_lo_u32 v5, v5, v2
	v_mul_hi_u32 v5, v2, v5
	v_add_u32_e32 v2, v2, v5
	s_waitcnt vmcnt(0)
	v_mul_hi_u32 v2, v4, v2
	v_mul_lo_u32 v5, v2, v3
	v_sub_u32_e32 v5, v4, v5
	v_add_u32_e32 v6, 1, v2
	v_cmp_ge_u32_e32 vcc, v5, v3
	v_add_u32_e32 v4, 1, v4
	s_nop 0
	v_cndmask_b32_e32 v2, v2, v6, vcc
	v_sub_u32_e32 v6, v5, v3
	v_cndmask_b32_e32 v5, v5, v6, vcc
	v_add_u32_e32 v6, 1, v2
	v_cmp_ge_u32_e32 vcc, v5, v3
	s_nop 1
	v_cndmask_b32_e32 v2, v2, v6, vcc
	v_mul_lo_u32 v5, v3, v2
	v_add_u32_e32 v3, v5, v3
	v_cmp_ne_u32_e32 vcc, v4, v3
	s_and_saveexec_b64 s[6:7], vcc
	s_xor_b64 s[6:7], exec, s[6:7]
	s_cbranch_execz .LBB0_182
	s_waitcnt lgkmcnt(0)
	v_add_u32_e32 v19, 1, v2
	v_mul_lo_u32 v19, v19, v1
	v_mov_b32_e32 v1, 0x7000
	global_load_dword v1, v1, s[90:91] offset:1024 sc1
	s_add_u32 s12, s90, 0x7400
	s_addc_u32 s13, s91, 0
	s_waitcnt vmcnt(0)
	v_cmp_lt_u32_e32 vcc, v1, v19
	s_and_saveexec_b64 s[8:9], vcc
	s_cbranch_execz .LBB0_181
	s_add_u32 s10, s90, 0x4200
	s_addc_u32 s11, s91, 0
	s_mov_b32 s3, 1
	s_mov_b64 s[14:15], 0
	v_mov_b32_e32 v1, 0
	s_branch .LBB0_172

; __device__ __forceinline__ unsigned xb_ld(unsigned* p)              { return __hip_atomic_load(p, __ATOMIC_RELAXED, __HIP_MEMORY_SCOPE_AGENT); }
; #define XB_SPIN(cond, bar) do { unsigned _sp = 0; while (cond) { __builtin_amdgcn_s_sleep(1); \
;     if ((++_sp & 255u) == 0u) { if (xb_ld(&(bar)[XB_TMO])) break; if (_sp > XB_SPIN_CAP) { atomicAdd(&(bar)[XB_TMO], 1u); break; } } } } while (0)
; __device__ __forceinline__ void xcd_barrier(const XcdBarrier& b) {
;     ...
;             XB_SPIN(xb_ld(&bar[XB_XGEN(b.x)]) == gen, bar);
.LBB0_176:
	global_load_dword v3, v1, s[12:13] sc1
	s_add_i32 s3, s3, 1
	s_mov_b64 s[46:47], -1
	s_waitcnt vmcnt(0)
	v_cmp_ge_u32_e32 vcc, v3, v19
	s_orn2_b64 s[28:29], vcc, exec
	s_branch .LBB0_171

; __device__ __forceinline__ unsigned xb_ld(unsigned* p)              { return __hip_atomic_load(p, __ATOMIC_RELAXED, __HIP_MEMORY_SCOPE_AGENT); }
; __device__ __forceinline__ unsigned xb_add(unsigned* p, unsigned v) { return __hip_atomic_fetch_add(p, v, __ATOMIC_RELAXED, __HIP_MEMORY_SCOPE_AGENT); }
; #define XB_SPIN(cond, bar) do { unsigned _sp = 0; while (cond) { __builtin_amdgcn_s_sleep(1); \
;     if ((++_sp & 255u) == 0u) { if (xb_ld(&(bar)[XB_TMO])) break; if (_sp > XB_SPIN_CAP) { atomicAdd(&(bar)[XB_TMO], 1u); break; } } } } while (0)
; __device__ __forceinline__ void xcd_barrier(const XcdBarrier& b) {
;     ...
;         if (old + 1u == (gen + 1u) * nloc) {
;             __builtin_amdgcn_fence(__ATOMIC_RELEASE, "agent");
;             asm volatile("s_waitcnt vmcnt(0)" ::: "memory");
;             const unsigned og = xb_add(&bar[XB_TOP], 1u);
;             const unsigned tg = og / nx;
;             if (og + 1u == (tg + 1u) * nx) xb_add(&bar[XB_TOPGEN], 1u);
;             else XB_SPIN(xb_ld(&bar[XB_TOPGEN]) == tg, bar);
.LBB0_182:
	s_andn2_saveexec_b64 s[6:7], s[6:7]
	s_cbranch_execz .LBB0_200
	s_mov_b64 s[6:7], exec
	v_add_u32_e32 v19, 1, v2
	v_mul_lo_u32 v19, v19, v1
	buffer_wbl2 sc1
	s_waitcnt lgkmcnt(0)
	s_waitcnt vmcnt(0)
	v_mbcnt_lo_u32_b32 v2, s6, 0
	v_mbcnt_hi_u32_b32 v2, s7, v2
	v_cmp_eq_u32_e32 vcc, 0, v2
	s_and_saveexec_b64 s[8:9], vcc
	s_cbranch_execz .LBB0_185
	s_bcnt1_i32_b64 s3, s[6:7]
	v_mov_b32_e32 v3, 0x7000
	v_mov_b32_e32 v4, s3
	global_atomic_add v3, v3, v4, s[90:91] offset:1024 sc0
.LBB0_185:
	s_or_b64 exec, exec, s[8:9]
	v_cvt_f32_u32_e32 v4, v1
	s_waitcnt vmcnt(0)
	v_readfirstlane_b32 s3, v3
	s_add_u32 s8, s90, 0x7400
	s_addc_u32 s9, s91, 0
	v_rcp_iflag_f32_e32 v4, v4
	v_add_u32_e32 v2, s3, v2
	v_add_u32_e32 v5, 1, v2
	s_mov_b64 s[10:11], -1
	v_mul_f32_e32 v3, 0x4f7ffffe, v4
	v_cvt_u32_f32_e32 v3, v3
	v_sub_u32_e32 v4, 0, v1
	v_mul_lo_u32 v4, v4, v3
	v_mul_hi_u32 v4, v3, v4
	v_add_u32_e32 v3, v3, v4
	v_mul_hi_u32 v3, v2, v3
	v_mul_lo_u32 v4, v3, v1
	v_sub_u32_e32 v2, v2, v4
	v_add_u32_e32 v6, 1, v3
	v_cmp_ge_u32_e32 vcc, v2, v1
	v_sub_u32_e32 v4, v2, v1
	s_nop 0
	v_cndmask_b32_e32 v3, v3, v6, vcc
	v_cndmask_b32_e32 v2, v2, v4, vcc
	v_add_u32_e32 v4, 1, v3
	v_cmp_ge_u32_e32 vcc, v2, v1
	s_nop 1
	v_cndmask_b32_e32 v4, v3, v4, vcc
	v_mul_lo_u32 v2, v1, v4
	v_add_u32_e32 v1, v2, v1
	v_cmp_ne_u32_e32 vcc, v5, v1
	v_mov_b64_e32 v[2:3], s[8:9]
	s_and_saveexec_b64 s[6:7], vcc
	s_cbranch_execz .LBB0_197
	v_mov_b32_e32 v1, 0
	global_load_dword v2, v1, s[8:9] sc1
	s_mov_b64 s[14:15], 0
	s_waitcnt vmcnt(0)
	v_cmp_lt_u32_e32 vcc, v2, v19
	s_and_saveexec_b64 s[12:13], vcc
	s_cbranch_execz .LBB0_196
	s_add_u32 s10, s90, 0x4200
	s_addc_u32 s11, s91, 0
	s_mov_b32 s3, 1
	s_branch .LBB0_189

; __device__ __forceinline__ unsigned xb_ld(unsigned* p)              { return __hip_atomic_load(p, __ATOMIC_RELAXED, __HIP_MEMORY_SCOPE_AGENT); }
; #define XB_SPIN(cond, bar) do { unsigned _sp = 0; while (cond) { __builtin_amdgcn_s_sleep(1); \
;     if ((++_sp & 255u) == 0u) { if (xb_ld(&(bar)[XB_TMO])) break; if (_sp > XB_SPIN_CAP) { atomicAdd(&(bar)[XB_TMO], 1u); break; } } } } while (0)
; __device__ __forceinline__ void xcd_barrier(const XcdBarrier& b) {
;     ...
;             else XB_SPIN(xb_ld(&bar[XB_TOPGEN]) == tg, bar);
.LBB0_193:
	global_load_dword v2, v1, s[8:9] sc1
	s_add_i32 s3, s3, 1
	s_mov_b64 s[28:29], -1
	s_waitcnt vmcnt(0)
	v_cmp_ge_u32_e32 vcc, v2, v19
	s_orn2_b64 s[52:53], vcc, exec
	s_branch .LBB0_188

; __device__ __forceinline__ unsigned xb_ld(unsigned* p)              { return __hip_atomic_load(p, __ATOMIC_RELAXED, __HIP_MEMORY_SCOPE_AGENT); }
; __device__ __forceinline__ unsigned xb_add(unsigned* p, unsigned v) { return __hip_atomic_fetch_add(p, v, __ATOMIC_RELAXED, __HIP_MEMORY_SCOPE_AGENT); }
; #define XB_SPIN(cond, bar) do { unsigned _sp = 0; while (cond) { __builtin_amdgcn_s_sleep(1); \
;     if ((++_sp & 255u) == 0u) { if (xb_ld(&(bar)[XB_TMO])) break; if (_sp > XB_SPIN_CAP) { atomicAdd(&(bar)[XB_TMO], 1u); break; } } } } while (0)
; __device__ __forceinline__ void xcd_barrier(const XcdBarrier& b) {
;     ...
;             if (og + 1u == (tg + 1u) * nx) xb_add(&bar[XB_TOPGEN], 1u);
;             else XB_SPIN(xb_ld(&bar[XB_TOPGEN]) == tg, bar);
;             __builtin_amdgcn_fence(__ATOMIC_ACQUIRE, "agent");
;             xb_add(&bar[XB_XGEN(b.x)], 1u);
;             asm volatile("s_waitcnt vmcnt(0)" ::: "memory");
;         } else {
;             XB_SPIN(xb_ld(&bar[XB_XGEN(b.x)]) == gen, bar);
;             __builtin_amdgcn_fence(__ATOMIC_ACQUIRE, "agent");
;             asm volatile("s_waitcnt vmcnt(0)" ::: "memory");
.LBB0_197:
	s_or_b64 exec, exec, s[6:7]
	s_and_saveexec_b64 s[6:7], s[10:11]
	s_cbranch_execz .LBB0_199
	v_mov_b32_e32 v1, 1
.LBB0_199:
	s_or_b64 exec, exec, s[6:7]
	v_mov_b32_e32 v1, 0x2000
	v_mov_b32_e32 v2, 1
	s_waitcnt vmcnt(0)
	buffer_inv sc1
	s_waitcnt vmcnt(0)

; __device__ __forceinline__ unsigned xb_ld(unsigned* p)              { return __hip_atomic_load(p, __ATOMIC_RELAXED, __HIP_MEMORY_SCOPE_AGENT); }
; __device__ __forceinline__ unsigned xb_add(unsigned* p, unsigned v) { return __hip_atomic_fetch_add(p, v, __ATOMIC_RELAXED, __HIP_MEMORY_SCOPE_AGENT); }
; #define XB_SPIN(cond, bar) do { unsigned _sp = 0; while (cond) { __builtin_amdgcn_s_sleep(1); \
;     if ((++_sp & 255u) == 0u) { if (xb_ld(&(bar)[XB_TMO])) break; if (_sp > XB_SPIN_CAP) { atomicAdd(&(bar)[XB_TMO], 1u); break; } } } } while (0)
; __device__ __forceinline__ void xcd_barrier(const XcdBarrier& b) {
;     ...
;             if (og + 1u == (tg + 1u) * nx) xb_add(&bar[XB_TOPGEN], 1u);
;             else XB_SPIN(xb_ld(&bar[XB_TOPGEN]) == tg, bar);
;             __builtin_amdgcn_fence(__ATOMIC_ACQUIRE, "agent");
;             xb_add(&bar[XB_XGEN(b.x)], 1u);
;             asm volatile("s_waitcnt vmcnt(0)" ::: "memory");
;         } else {
;             XB_SPIN(xb_ld(&bar[XB_XGEN(b.x)]) == gen, bar);
;             __builtin_amdgcn_fence(__ATOMIC_ACQUIRE, "agent");
;             asm volatile("s_waitcnt vmcnt(0)" ::: "memory");
.LBB0_306:
	s_or_b64 exec, exec, s[6:7]
	s_and_saveexec_b64 s[6:7], s[10:11]
	s_cbranch_execz .LBB0_308
	v_mov_b32_e32 v1, 1
.LBB0_308:
	s_or_b64 exec, exec, s[6:7]
	v_mov_b32_e32 v1, 0x2000
	v_mov_b32_e32 v2, 1
	s_waitcnt vmcnt(0)
	buffer_inv sc1
	s_waitcnt vmcnt(0)

; __device__ __forceinline__ unsigned xb_ld(unsigned* p)              { return __hip_atomic_load(p, __ATOMIC_RELAXED, __HIP_MEMORY_SCOPE_AGENT); }
; #define XB_SPIN(cond, bar) do { unsigned _sp = 0; while (cond) { __builtin_amdgcn_s_sleep(1); \
;     if ((++_sp & 255u) == 0u) { if (xb_ld(&(bar)[XB_TMO])) break; if (_sp > XB_SPIN_CAP) { atomicAdd(&(bar)[XB_TMO], 1u); break; } } } } while (0)
; __device__ __forceinline__ void xcd_barrier(const XcdBarrier& b) {
;     ...
;             XB_SPIN(xb_ld(&bar[XB_XGEN(b.x)]) == gen, bar);
.LBB0_402:
	global_load_dword v3, v1, s[12:13] sc1
	s_add_i32 s3, s3, 1
	s_mov_b64 s[30:31], -1
	s_waitcnt vmcnt(0)
	v_cmp_ge_u32_e32 vcc, v3, v19
	s_orn2_b64 s[28:29], vcc, exec
	s_branch .LBB0_397

; __device__ __forceinline__ unsigned xb_ld(unsigned* p)              { return __hip_atomic_load(p, __ATOMIC_RELAXED, __HIP_MEMORY_SCOPE_AGENT); }
; #define XB_SPIN(cond, bar) do { unsigned _sp = 0; while (cond) { __builtin_amdgcn_s_sleep(1); \
;     if ((++_sp & 255u) == 0u) { if (xb_ld(&(bar)[XB_TMO])) break; if (_sp > XB_SPIN_CAP) { atomicAdd(&(bar)[XB_TMO], 1u); break; } } } } while (0)
; __device__ __forceinline__ void xcd_barrier(const XcdBarrier& b) {
;     ...
;             else XB_SPIN(xb_ld(&bar[XB_TOPGEN]) == tg, bar);
.LBB0_419:
	global_load_dword v2, v1, s[8:9] sc1
	s_add_i32 s3, s3, 1
	s_mov_b64 s[28:29], -1
	s_waitcnt vmcnt(0)
	v_cmp_ge_u32_e32 vcc, v2, v19
	s_orn2_b64 s[46:47], vcc, exec
	s_branch .LBB0_414

; __device__ __forceinline__ unsigned xb_ld(unsigned* p)              { return __hip_atomic_load(p, __ATOMIC_RELAXED, __HIP_MEMORY_SCOPE_AGENT); }
; __device__ __forceinline__ unsigned xb_add(unsigned* p, unsigned v) { return __hip_atomic_fetch_add(p, v, __ATOMIC_RELAXED, __HIP_MEMORY_SCOPE_AGENT); }
; #define XB_SPIN(cond, bar) do { unsigned _sp = 0; while (cond) { __builtin_amdgcn_s_sleep(1); \
;     if ((++_sp & 255u) == 0u) { if (xb_ld(&(bar)[XB_TMO])) break; if (_sp > XB_SPIN_CAP) { atomicAdd(&(bar)[XB_TMO], 1u); break; } } } } while (0)
; __device__ __forceinline__ void xcd_barrier(const XcdBarrier& b) {
;     ...
;             if (og + 1u == (tg + 1u) * nx) xb_add(&bar[XB_TOPGEN], 1u);
;             else XB_SPIN(xb_ld(&bar[XB_TOPGEN]) == tg, bar);
;             __builtin_amdgcn_fence(__ATOMIC_ACQUIRE, "agent");
;             xb_add(&bar[XB_XGEN(b.x)], 1u);
;             asm volatile("s_waitcnt vmcnt(0)" ::: "memory");
;         } else {
;             XB_SPIN(xb_ld(&bar[XB_XGEN(b.x)]) == gen, bar);
;             __builtin_amdgcn_fence(__ATOMIC_ACQUIRE, "agent");
;             asm volatile("s_waitcnt vmcnt(0)" ::: "memory");
.LBB0_423:
	s_or_b64 exec, exec, s[6:7]
	s_and_saveexec_b64 s[6:7], s[10:11]
	s_cbranch_execz .LBB0_425
	v_mov_b32_e32 v1, 1
.LBB0_425:
	s_or_b64 exec, exec, s[6:7]
	v_mov_b32_e32 v1, 0x2000
	v_mov_b32_e32 v2, 1
	s_waitcnt vmcnt(0)
	buffer_inv sc1
	s_waitcnt vmcnt(0)

; __device__ __forceinline__ unsigned xb_ld(unsigned* p)              { return __hip_atomic_load(p, __ATOMIC_RELAXED, __HIP_MEMORY_SCOPE_AGENT); }
; #define XB_SPIN(cond, bar) do { unsigned _sp = 0; while (cond) { __builtin_amdgcn_s_sleep(1); \
;     if ((++_sp & 255u) == 0u) { if (xb_ld(&(bar)[XB_TMO])) break; if (_sp > XB_SPIN_CAP) { atomicAdd(&(bar)[XB_TMO], 1u); break; } } } } while (0)
; __device__ __forceinline__ void xcd_barrier(const XcdBarrier& b) {
;     ...
;             XB_SPIN(xb_ld(&bar[XB_XGEN(b.x)]) == gen, bar);
.LBB0_780:
	global_load_dword v3, v1, s[12:13] sc1
	s_add_i32 s3, s3, 1
	s_mov_b64 s[20:21], -1
	s_waitcnt vmcnt(0)
	v_cmp_ge_u32_e32 vcc, v3, v19
	s_orn2_b64 s[18:19], vcc, exec
	s_branch .LBB0_775

; __device__ __forceinline__ unsigned xb_ld(unsigned* p)              { return __hip_atomic_load(p, __ATOMIC_RELAXED, __HIP_MEMORY_SCOPE_AGENT); }
; #define XB_SPIN(cond, bar) do { unsigned _sp = 0; while (cond) { __builtin_amdgcn_s_sleep(1); \
;     if ((++_sp & 255u) == 0u) { if (xb_ld(&(bar)[XB_TMO])) break; if (_sp > XB_SPIN_CAP) { atomicAdd(&(bar)[XB_TMO], 1u); break; } } } } while (0)
; __device__ __forceinline__ void xcd_barrier(const XcdBarrier& b) {
;     ...
;             else XB_SPIN(xb_ld(&bar[XB_TOPGEN]) == tg, bar);
.LBB0_797:
	global_load_dword v2, v1, s[8:9] sc1
	s_add_i32 s3, s3, 1
	s_mov_b64 s[18:19], -1
	s_waitcnt vmcnt(0)
	v_cmp_ge_u32_e32 vcc, v2, v19
	s_orn2_b64 s[28:29], vcc, exec
	s_branch .LBB0_792

; __device__ __forceinline__ unsigned xb_ld(unsigned* p)              { return __hip_atomic_load(p, __ATOMIC_RELAXED, __HIP_MEMORY_SCOPE_AGENT); }
; __device__ __forceinline__ unsigned xb_add(unsigned* p, unsigned v) { return __hip_atomic_fetch_add(p, v, __ATOMIC_RELAXED, __HIP_MEMORY_SCOPE_AGENT); }
; #define XB_SPIN(cond, bar) do { unsigned _sp = 0; while (cond) { __builtin_amdgcn_s_sleep(1); \
;     if ((++_sp & 255u) == 0u) { if (xb_ld(&(bar)[XB_TMO])) break; if (_sp > XB_SPIN_CAP) { atomicAdd(&(bar)[XB_TMO], 1u); break; } } } } while (0)
; __device__ __forceinline__ void xcd_barrier(const XcdBarrier& b) {
;     ...
;             if (og + 1u == (tg + 1u) * nx) xb_add(&bar[XB_TOPGEN], 1u);
;             else XB_SPIN(xb_ld(&bar[XB_TOPGEN]) == tg, bar);
;             __builtin_amdgcn_fence(__ATOMIC_ACQUIRE, "agent");
;             xb_add(&bar[XB_XGEN(b.x)], 1u);
;             asm volatile("s_waitcnt vmcnt(0)" ::: "memory");
;         } else {
;             XB_SPIN(xb_ld(&bar[XB_XGEN(b.x)]) == gen, bar);
;             __builtin_amdgcn_fence(__ATOMIC_ACQUIRE, "agent");
;             asm volatile("s_waitcnt vmcnt(0)" ::: "memory");
.LBB0_801:
	s_or_b64 exec, exec, s[6:7]
	s_and_saveexec_b64 s[6:7], s[10:11]
	s_cbranch_execz .LBB0_803
	v_mov_b32_e32 v1, 1
.LBB0_803:
	s_or_b64 exec, exec, s[6:7]
	v_mov_b32_e32 v1, 0x2000
	v_mov_b32_e32 v2, 1
	s_waitcnt vmcnt(0)
	buffer_inv sc1
	s_waitcnt vmcnt(0)

; __device__ __forceinline__ unsigned xb_ld(unsigned* p)              { return __hip_atomic_load(p, __ATOMIC_RELAXED, __HIP_MEMORY_SCOPE_AGENT); }
; __device__ __forceinline__ unsigned xb_add(unsigned* p, unsigned v) { return __hip_atomic_fetch_add(p, v, __ATOMIC_RELAXED, __HIP_MEMORY_SCOPE_AGENT); }
; #define XB_SPIN(cond, bar) do { unsigned _sp = 0; while (cond) { __builtin_amdgcn_s_sleep(1); \
;     if ((++_sp & 255u) == 0u) { if (xb_ld(&(bar)[XB_TMO])) break; if (_sp > XB_SPIN_CAP) { atomicAdd(&(bar)[XB_TMO], 1u); break; } } } } while (0)
; __device__ __forceinline__ void xcd_barrier(const XcdBarrier& b) {
;     ...
;             if (og + 1u == (tg + 1u) * nx) xb_add(&bar[XB_TOPGEN], 1u);
;             else XB_SPIN(xb_ld(&bar[XB_TOPGEN]) == tg, bar);
;             __builtin_amdgcn_fence(__ATOMIC_ACQUIRE, "agent");
;             xb_add(&bar[XB_XGEN(b.x)], 1u);
;             asm volatile("s_waitcnt vmcnt(0)" ::: "memory");
;         } else {
;             XB_SPIN(xb_ld(&bar[XB_XGEN(b.x)]) == gen, bar);
;             __builtin_amdgcn_fence(__ATOMIC_ACQUIRE, "agent");
;             asm volatile("s_waitcnt vmcnt(0)" ::: "memory");
.LBB0_881:
	s_or_b64 exec, exec, s[6:7]
	s_and_saveexec_b64 s[6:7], s[10:11]
	s_cbranch_execz .LBB0_883
	v_mov_b32_e32 v1, 1
.LBB0_883:
	s_or_b64 exec, exec, s[6:7]
	v_mov_b32_e32 v1, 0x2000
	v_mov_b32_e32 v2, 1
	s_waitcnt vmcnt(0)
	buffer_inv sc1
	s_waitcnt vmcnt(0)

; __device__ __forceinline__ unsigned xb_ld(unsigned* p)              { return __hip_atomic_load(p, __ATOMIC_RELAXED, __HIP_MEMORY_SCOPE_AGENT); }
; __device__ __forceinline__ unsigned xb_add(unsigned* p, unsigned v) { return __hip_atomic_fetch_add(p, v, __ATOMIC_RELAXED, __HIP_MEMORY_SCOPE_AGENT); }
; #define XB_SPIN(cond, bar) do { unsigned _sp = 0; while (cond) { __builtin_amdgcn_s_sleep(1); \
;     if ((++_sp & 255u) == 0u) { if (xb_ld(&(bar)[XB_TMO])) break; if (_sp > XB_SPIN_CAP) { atomicAdd(&(bar)[XB_TMO], 1u); break; } } } } while (0)
; __device__ __forceinline__ void xcd_barrier(const XcdBarrier& b) {
;     ...
;             if (og + 1u == (tg + 1u) * nx) xb_add(&bar[XB_TOPGEN], 1u);
;             else XB_SPIN(xb_ld(&bar[XB_TOPGEN]) == tg, bar);
;             __builtin_amdgcn_fence(__ATOMIC_ACQUIRE, "agent");
;             xb_add(&bar[XB_XGEN(b.x)], 1u);
;             asm volatile("s_waitcnt vmcnt(0)" ::: "memory");
;         } else {
;             XB_SPIN(xb_ld(&bar[XB_XGEN(b.x)]) == gen, bar);
;             __builtin_amdgcn_fence(__ATOMIC_ACQUIRE, "agent");
;             asm volatile("s_waitcnt vmcnt(0)" ::: "memory");
.LBB0_941:
	s_or_b64 exec, exec, s[6:7]
	s_and_saveexec_b64 s[6:7], s[10:11]
	s_cbranch_execz .LBB0_943
	v_mov_b32_e32 v1, 1
.LBB0_943:
	s_or_b64 exec, exec, s[6:7]
	v_mov_b32_e32 v1, 0x2000
	v_mov_b32_e32 v2, 1
	s_waitcnt vmcnt(0)
	buffer_inv sc1
	s_waitcnt vmcnt(0)

; __device__ __forceinline__ unsigned xb_ld(unsigned* p)              { return __hip_atomic_load(p, __ATOMIC_RELAXED, __HIP_MEMORY_SCOPE_AGENT); }
; __device__ __forceinline__ unsigned xb_add(unsigned* p, unsigned v) { return __hip_atomic_fetch_add(p, v, __ATOMIC_RELAXED, __HIP_MEMORY_SCOPE_AGENT); }
; #define XB_SPIN(cond, bar) do { unsigned _sp = 0; while (cond) { __builtin_amdgcn_s_sleep(1); \
;     if ((++_sp & 255u) == 0u) { if (xb_ld(&(bar)[XB_TMO])) break; if (_sp > XB_SPIN_CAP) { atomicAdd(&(bar)[XB_TMO], 1u); break; } } } } while (0)
; __device__ __forceinline__ void xcd_barrier(const XcdBarrier& b) {
;     ...
;             if (og + 1u == (tg + 1u) * nx) xb_add(&bar[XB_TOPGEN], 1u);
;             else XB_SPIN(xb_ld(&bar[XB_TOPGEN]) == tg, bar);
;             __builtin_amdgcn_fence(__ATOMIC_ACQUIRE, "agent");
;             xb_add(&bar[XB_XGEN(b.x)], 1u);
;             asm volatile("s_waitcnt vmcnt(0)" ::: "memory");
;         } else {
;             XB_SPIN(xb_ld(&bar[XB_XGEN(b.x)]) == gen, bar);
;             __builtin_amdgcn_fence(__ATOMIC_ACQUIRE, "agent");
;             asm volatile("s_waitcnt vmcnt(0)" ::: "memory");
.LBB0_1023:
	s_or_b64 exec, exec, s[6:7]
	s_and_saveexec_b64 s[6:7], s[10:11]
	s_cbranch_execz .LBB0_1025
	v_mov_b32_e32 v1, 1
.LBB0_1025:
	s_or_b64 exec, exec, s[6:7]
	v_mov_b32_e32 v1, 0x2000
	v_mov_b32_e32 v2, 1
	s_waitcnt vmcnt(0)
	buffer_inv sc1
	s_waitcnt vmcnt(0)

; __device__ __forceinline__ unsigned xb_ld(unsigned* p)              { return __hip_atomic_load(p, __ATOMIC_RELAXED, __HIP_MEMORY_SCOPE_AGENT); }
; __device__ __forceinline__ unsigned xb_add(unsigned* p, unsigned v) { return __hip_atomic_fetch_add(p, v, __ATOMIC_RELAXED, __HIP_MEMORY_SCOPE_AGENT); }
; #define XB_SPIN(cond, bar) do { unsigned _sp = 0; while (cond) { __builtin_amdgcn_s_sleep(1); \
;     if ((++_sp & 255u) == 0u) { if (xb_ld(&(bar)[XB_TMO])) break; if (_sp > XB_SPIN_CAP) { atomicAdd(&(bar)[XB_TMO], 1u); break; } } } } while (0)
; __device__ __forceinline__ void xcd_barrier(const XcdBarrier& b) {
;     ...
;             if (og + 1u == (tg + 1u) * nx) xb_add(&bar[XB_TOPGEN], 1u);
;             else XB_SPIN(xb_ld(&bar[XB_TOPGEN]) == tg, bar);
;             __builtin_amdgcn_fence(__ATOMIC_ACQUIRE, "agent");
;             xb_add(&bar[XB_XGEN(b.x)], 1u);
;             asm volatile("s_waitcnt vmcnt(0)" ::: "memory");
;         } else {
;             XB_SPIN(xb_ld(&bar[XB_XGEN(b.x)]) == gen, bar);
;             __builtin_amdgcn_fence(__ATOMIC_ACQUIRE, "agent");
;             asm volatile("s_waitcnt vmcnt(0)" ::: "memory");
.LBB0_1087:
	s_or_b64 exec, exec, s[6:7]
	s_and_saveexec_b64 s[6:7], s[10:11]
	s_cbranch_execz .LBB0_1089
	v_mov_b32_e32 v1, 1
.LBB0_1089:
	s_or_b64 exec, exec, s[6:7]
	v_mov_b32_e32 v1, 0x2000
	v_mov_b32_e32 v2, 1
	s_waitcnt vmcnt(0)
	buffer_inv sc1
	s_waitcnt vmcnt(0)

; __device__ __forceinline__ unsigned xb_ld(unsigned* p)              { return __hip_atomic_load(p, __ATOMIC_RELAXED, __HIP_MEMORY_SCOPE_AGENT); }
; __device__ __forceinline__ unsigned xb_add(unsigned* p, unsigned v) { return __hip_atomic_fetch_add(p, v, __ATOMIC_RELAXED, __HIP_MEMORY_SCOPE_AGENT); }
; #define XB_SPIN(cond, bar) do { unsigned _sp = 0; while (cond) { __builtin_amdgcn_s_sleep(1); \
;     if ((++_sp & 255u) == 0u) { if (xb_ld(&(bar)[XB_TMO])) break; if (_sp > XB_SPIN_CAP) { atomicAdd(&(bar)[XB_TMO], 1u); break; } } } } while (0)
; __device__ __forceinline__ void xcd_barrier(const XcdBarrier& b) {
;     ...
;             if (og + 1u == (tg + 1u) * nx) xb_add(&bar[XB_TOPGEN], 1u);
;             else XB_SPIN(xb_ld(&bar[XB_TOPGEN]) == tg, bar);
;             __builtin_amdgcn_fence(__ATOMIC_ACQUIRE, "agent");
;             xb_add(&bar[XB_XGEN(b.x)], 1u);
;             asm volatile("s_waitcnt vmcnt(0)" ::: "memory");
;         } else {
;             XB_SPIN(xb_ld(&bar[XB_XGEN(b.x)]) == gen, bar);
;             __builtin_amdgcn_fence(__ATOMIC_ACQUIRE, "agent");
;             asm volatile("s_waitcnt vmcnt(0)" ::: "memory");
.LBB0_1162:
	s_or_b64 exec, exec, s[6:7]
	s_and_saveexec_b64 s[6:7], s[10:11]
	s_cbranch_execz .LBB0_1164
	v_mov_b32_e32 v1, 1
.LBB0_1164:
	s_or_b64 exec, exec, s[6:7]
	v_mov_b32_e32 v1, 0x2000
	v_mov_b32_e32 v2, 1
	s_waitcnt vmcnt(0)
	buffer_inv sc1
	s_waitcnt vmcnt(0)

; __device__ __forceinline__ unsigned xb_ld(unsigned* p)              { return __hip_atomic_load(p, __ATOMIC_RELAXED, __HIP_MEMORY_SCOPE_AGENT); }
; __device__ __forceinline__ unsigned xb_add(unsigned* p, unsigned v) { return __hip_atomic_fetch_add(p, v, __ATOMIC_RELAXED, __HIP_MEMORY_SCOPE_AGENT); }
; #define XB_SPIN(cond, bar) do { unsigned _sp = 0; while (cond) { __builtin_amdgcn_s_sleep(1); \
;     if ((++_sp & 255u) == 0u) { if (xb_ld(&(bar)[XB_TMO])) break; if (_sp > XB_SPIN_CAP) { atomicAdd(&(bar)[XB_TMO], 1u); break; } } } } while (0)
; __device__ __forceinline__ void xcd_barrier(const XcdBarrier& b) {
;     ...
;         const unsigned old = xb_add(&bar[XB_XSUB(b.x)], 1u);
;         const unsigned gen = old / nloc;
;         if (old + 1u == (gen + 1u) * nloc) {
;             __builtin_amdgcn_fence(__ATOMIC_RELEASE, "agent");
;             asm volatile("s_waitcnt vmcnt(0)" ::: "memory");
;             const unsigned og = xb_add(&bar[XB_TOP], 1u);
;             const unsigned tg = og / nx;
;             if (og + 1u == (tg + 1u) * nx) xb_add(&bar[XB_TOPGEN], 1u);
;             else XB_SPIN(xb_ld(&bar[XB_TOPGEN]) == tg, bar);
;             __builtin_amdgcn_fence(__ATOMIC_ACQUIRE, "agent");
;             xb_add(&bar[XB_XGEN(b.x)], 1u);
;             asm volatile("s_waitcnt vmcnt(0)" ::: "memory");
;         } else {
;             XB_SPIN(xb_ld(&bar[XB_XGEN(b.x)]) == gen, bar);
.LBB0_1196:
	s_lshl_b32 s3, s82, 8
	s_add_u32 s8, s80, s3
	s_addc_u32 s9, s81, 0
	v_mov_b32_e32 v2, 0x1000
	v_mov_b32_e32 v4, 1
	global_atomic_add v4, v2, v4, s[8:9] offset:1024 sc0
	v_cvt_f32_u32_e32 v2, v3
	v_sub_u32_e32 v5, 0, v3
	v_rcp_iflag_f32_e32 v2, v2
	s_nop 0
	v_mul_f32_e32 v2, 0x4f7ffffe, v2
	v_cvt_u32_f32_e32 v2, v2
	v_mul_lo_u32 v5, v5, v2
	v_mul_hi_u32 v5, v2, v5
	v_add_u32_e32 v2, v2, v5
	s_waitcnt vmcnt(0)
	v_mul_hi_u32 v2, v4, v2
	v_mul_lo_u32 v5, v2, v3
	v_sub_u32_e32 v5, v4, v5
	v_add_u32_e32 v6, 1, v2
	v_cmp_ge_u32_e32 vcc, v5, v3
	v_add_u32_e32 v4, 1, v4
	s_nop 0
	v_cndmask_b32_e32 v2, v2, v6, vcc
	v_sub_u32_e32 v6, v5, v3
	v_cndmask_b32_e32 v5, v5, v6, vcc
	v_add_u32_e32 v6, 1, v2
	v_cmp_ge_u32_e32 vcc, v5, v3
	s_nop 1
	v_cndmask_b32_e32 v2, v2, v6, vcc
	v_mul_lo_u32 v5, v3, v2
	v_add_u32_e32 v3, v5, v3
	v_cmp_ne_u32_e32 vcc, v4, v3
	s_and_saveexec_b64 s[10:11], vcc
	s_xor_b64 s[10:11], exec, s[10:11]
	s_cbranch_execz .LBB0_1210
	s_waitcnt lgkmcnt(0)
	v_add_u32_e32 v19, 1, v2
	v_mul_lo_u32 v19, v19, v1
	v_mov_b32_e32 v1, 0x7000
	global_load_dword v1, v1, s[90:91] offset:1024 sc1
	s_add_u32 s16, s90, 0x7400
	s_addc_u32 s17, s91, 0
	s_waitcnt vmcnt(0)
	v_cmp_lt_u32_e32 vcc, v1, v19
	s_and_saveexec_b64 s[12:13], vcc
	s_cbranch_execz .LBB0_1209
	s_add_u32 s14, s90, 0x4200
	s_addc_u32 s15, s91, 0
	s_mov_b32 s3, 1
	s_mov_b64 s[18:19], 0
	v_mov_b32_e32 v1, 0
	s_branch .LBB0_1200

; __device__ __forceinline__ unsigned xb_ld(unsigned* p)              { return __hip_atomic_load(p, __ATOMIC_RELAXED, __HIP_MEMORY_SCOPE_AGENT); }
; #define XB_SPIN(cond, bar) do { unsigned _sp = 0; while (cond) { __builtin_amdgcn_s_sleep(1); \
;     if ((++_sp & 255u) == 0u) { if (xb_ld(&(bar)[XB_TMO])) break; if (_sp > XB_SPIN_CAP) { atomicAdd(&(bar)[XB_TMO], 1u); break; } } } } while (0)
; __device__ __forceinline__ void xcd_barrier(const XcdBarrier& b) {
;     ...
;             XB_SPIN(xb_ld(&bar[XB_XGEN(b.x)]) == gen, bar);
.LBB0_1204:
	global_load_dword v3, v1, s[16:17] sc1
	s_add_i32 s3, s3, 1
	s_mov_b64 s[30:31], -1
	s_waitcnt vmcnt(0)
	v_cmp_ge_u32_e32 vcc, v3, v19
	s_orn2_b64 s[28:29], vcc, exec
	s_branch .LBB0_1199

; __device__ __forceinline__ unsigned xb_ld(unsigned* p)              { return __hip_atomic_load(p, __ATOMIC_RELAXED, __HIP_MEMORY_SCOPE_AGENT); }
; __device__ __forceinline__ unsigned xb_add(unsigned* p, unsigned v) { return __hip_atomic_fetch_add(p, v, __ATOMIC_RELAXED, __HIP_MEMORY_SCOPE_AGENT); }
; #define XB_SPIN(cond, bar) do { unsigned _sp = 0; while (cond) { __builtin_amdgcn_s_sleep(1); \
;     if ((++_sp & 255u) == 0u) { if (xb_ld(&(bar)[XB_TMO])) break; if (_sp > XB_SPIN_CAP) { atomicAdd(&(bar)[XB_TMO], 1u); break; } } } } while (0)
; __device__ __forceinline__ void xcd_barrier(const XcdBarrier& b) {
;     ...
;         if (old + 1u == (gen + 1u) * nloc) {
;             __builtin_amdgcn_fence(__ATOMIC_RELEASE, "agent");
;             asm volatile("s_waitcnt vmcnt(0)" ::: "memory");
;             const unsigned og = xb_add(&bar[XB_TOP], 1u);
;             const unsigned tg = og / nx;
;             if (og + 1u == (tg + 1u) * nx) xb_add(&bar[XB_TOPGEN], 1u);
;             else XB_SPIN(xb_ld(&bar[XB_TOPGEN]) == tg, bar);
.LBB0_1210:
	s_andn2_saveexec_b64 s[10:11], s[10:11]
	s_cbranch_execz .LBB0_1228
	s_mov_b64 s[10:11], exec
	v_add_u32_e32 v19, 1, v2
	v_mul_lo_u32 v19, v19, v1
	buffer_wbl2 sc1
	s_waitcnt lgkmcnt(0)
	s_waitcnt vmcnt(0)
	v_mbcnt_lo_u32_b32 v2, s10, 0
	v_mbcnt_hi_u32_b32 v2, s11, v2
	v_cmp_eq_u32_e32 vcc, 0, v2
	s_and_saveexec_b64 s[12:13], vcc
	s_cbranch_execz .LBB0_1213
	s_bcnt1_i32_b64 s3, s[10:11]
	v_mov_b32_e32 v3, 0x7000
	v_mov_b32_e32 v4, s3
	global_atomic_add v3, v3, v4, s[90:91] offset:1024 sc0
.LBB0_1213:
	s_or_b64 exec, exec, s[12:13]
	v_cvt_f32_u32_e32 v4, v1
	s_waitcnt vmcnt(0)
	v_readfirstlane_b32 s3, v3
	s_add_u32 s12, s90, 0x7400
	s_addc_u32 s13, s91, 0
	v_rcp_iflag_f32_e32 v4, v4
	v_add_u32_e32 v2, s3, v2
	v_add_u32_e32 v5, 1, v2
	s_mov_b64 s[14:15], -1
	v_mul_f32_e32 v3, 0x4f7ffffe, v4
	v_cvt_u32_f32_e32 v3, v3
	v_sub_u32_e32 v4, 0, v1
	v_mul_lo_u32 v4, v4, v3
	v_mul_hi_u32 v4, v3, v4
	v_add_u32_e32 v3, v3, v4
	v_mul_hi_u32 v3, v2, v3
	v_mul_lo_u32 v4, v3, v1
	v_sub_u32_e32 v2, v2, v4
	v_add_u32_e32 v6, 1, v3
	v_cmp_ge_u32_e32 vcc, v2, v1
	v_sub_u32_e32 v4, v2, v1
	s_nop 0
	v_cndmask_b32_e32 v3, v3, v6, vcc
	v_cndmask_b32_e32 v2, v2, v4, vcc
	v_add_u32_e32 v4, 1, v3
	v_cmp_ge_u32_e32 vcc, v2, v1
	s_nop 1
	v_cndmask_b32_e32 v4, v3, v4, vcc
	v_mul_lo_u32 v2, v1, v4
	v_add_u32_e32 v1, v2, v1
	v_cmp_ne_u32_e32 vcc, v5, v1
	v_mov_b64_e32 v[2:3], s[12:13]
	s_and_saveexec_b64 s[10:11], vcc
	s_cbranch_execz .LBB0_1225
	v_mov_b32_e32 v1, 0
	global_load_dword v2, v1, s[12:13] sc1
	s_mov_b64 s[18:19], 0
	s_waitcnt vmcnt(0)
	v_cmp_lt_u32_e32 vcc, v2, v19
	s_and_saveexec_b64 s[16:17], vcc
	s_cbranch_execz .LBB0_1224
	s_add_u32 s14, s90, 0x4200
	s_addc_u32 s15, s91, 0
	s_mov_b32 s3, 1
	s_branch .LBB0_1217

; __device__ __forceinline__ unsigned xb_ld(unsigned* p)              { return __hip_atomic_load(p, __ATOMIC_RELAXED, __HIP_MEMORY_SCOPE_AGENT); }
; #define XB_SPIN(cond, bar) do { unsigned _sp = 0; while (cond) { __builtin_amdgcn_s_sleep(1); \
;     if ((++_sp & 255u) == 0u) { if (xb_ld(&(bar)[XB_TMO])) break; if (_sp > XB_SPIN_CAP) { atomicAdd(&(bar)[XB_TMO], 1u); break; } } } } while (0)
; __device__ __forceinline__ void xcd_barrier(const XcdBarrier& b) {
;     ...
;             else XB_SPIN(xb_ld(&bar[XB_TOPGEN]) == tg, bar);
.LBB0_1221:
	global_load_dword v2, v1, s[12:13] sc1
	s_add_i32 s3, s3, 1
	s_mov_b64 s[28:29], -1
	s_waitcnt vmcnt(0)
	v_cmp_ge_u32_e32 vcc, v2, v19
	s_orn2_b64 s[46:47], vcc, exec
	s_branch .LBB0_1216

; __device__ __forceinline__ unsigned xb_ld(unsigned* p)              { return __hip_atomic_load(p, __ATOMIC_RELAXED, __HIP_MEMORY_SCOPE_AGENT); }
; __device__ __forceinline__ unsigned xb_add(unsigned* p, unsigned v) { return __hip_atomic_fetch_add(p, v, __ATOMIC_RELAXED, __HIP_MEMORY_SCOPE_AGENT); }
; #define XB_SPIN(cond, bar) do { unsigned _sp = 0; while (cond) { __builtin_amdgcn_s_sleep(1); \
;     if ((++_sp & 255u) == 0u) { if (xb_ld(&(bar)[XB_TMO])) break; if (_sp > XB_SPIN_CAP) { atomicAdd(&(bar)[XB_TMO], 1u); break; } } } } while (0)
; __device__ __forceinline__ void xcd_barrier(const XcdBarrier& b) {
;     ...
;             if (og + 1u == (tg + 1u) * nx) xb_add(&bar[XB_TOPGEN], 1u);
;             else XB_SPIN(xb_ld(&bar[XB_TOPGEN]) == tg, bar);
;             __builtin_amdgcn_fence(__ATOMIC_ACQUIRE, "agent");
;             xb_add(&bar[XB_XGEN(b.x)], 1u);
;             asm volatile("s_waitcnt vmcnt(0)" ::: "memory");
;         } else {
;             XB_SPIN(xb_ld(&bar[XB_XGEN(b.x)]) == gen, bar);
;             __builtin_amdgcn_fence(__ATOMIC_ACQUIRE, "agent");
;             asm volatile("s_waitcnt vmcnt(0)" ::: "memory");
.LBB0_1225:
	s_or_b64 exec, exec, s[10:11]
	s_and_saveexec_b64 s[10:11], s[14:15]
	s_cbranch_execz .LBB0_1227
	v_mov_b32_e32 v1, 1
.LBB0_1227:
	s_or_b64 exec, exec, s[10:11]
	v_mov_b32_e32 v1, 0x2000
	v_mov_b32_e32 v2, 1
	s_waitcnt vmcnt(0)
	buffer_inv sc1
	s_waitcnt vmcnt(0)

; __device__ __forceinline__ unsigned xb_ld(unsigned* p)              { return __hip_atomic_load(p, __ATOMIC_RELAXED, __HIP_MEMORY_SCOPE_AGENT); }
; __device__ __forceinline__ unsigned xb_add(unsigned* p, unsigned v) { return __hip_atomic_fetch_add(p, v, __ATOMIC_RELAXED, __HIP_MEMORY_SCOPE_AGENT); }
; #define XB_SPIN(cond, bar) do { unsigned _sp = 0; while (cond) { __builtin_amdgcn_s_sleep(1); \
;     if ((++_sp & 255u) == 0u) { if (xb_ld(&(bar)[XB_TMO])) break; if (_sp > XB_SPIN_CAP) { atomicAdd(&(bar)[XB_TMO], 1u); break; } } } } while (0)
; __device__ __forceinline__ void xcd_barrier(const XcdBarrier& b) {
;     ...
;         const unsigned old = xb_add(&bar[XB_XSUB(b.x)], 1u);
;         const unsigned gen = old / nloc;
;         if (old + 1u == (gen + 1u) * nloc) {
;             __builtin_amdgcn_fence(__ATOMIC_RELEASE, "agent");
;             asm volatile("s_waitcnt vmcnt(0)" ::: "memory");
;             const unsigned og = xb_add(&bar[XB_TOP], 1u);
;             const unsigned tg = og / nx;
;             if (og + 1u == (tg + 1u) * nx) xb_add(&bar[XB_TOPGEN], 1u);
;             else XB_SPIN(xb_ld(&bar[XB_TOPGEN]) == tg, bar);
;             __builtin_amdgcn_fence(__ATOMIC_ACQUIRE, "agent");
;             xb_add(&bar[XB_XGEN(b.x)], 1u);
;             asm volatile("s_waitcnt vmcnt(0)" ::: "memory");
;         } else {
;             XB_SPIN(xb_ld(&bar[XB_XGEN(b.x)]) == gen, bar);
.LBB0_1262:
	s_lshl_b32 s0, s82, 8
	s_add_u32 s0, s80, s0
	s_addc_u32 s1, s81, 0
	v_mov_b32_e32 v2, 0x1000
	v_mov_b32_e32 v4, 1
	global_atomic_add v4, v2, v4, s[0:1] offset:1024 sc0
	v_cvt_f32_u32_e32 v2, v3
	v_sub_u32_e32 v5, 0, v3
	v_rcp_iflag_f32_e32 v2, v2
	s_nop 0
	v_mul_f32_e32 v2, 0x4f7ffffe, v2
	v_cvt_u32_f32_e32 v2, v2
	v_mul_lo_u32 v5, v5, v2
	v_mul_hi_u32 v5, v2, v5
	v_add_u32_e32 v2, v2, v5
	s_waitcnt vmcnt(0)
	v_mul_hi_u32 v2, v4, v2
	v_mul_lo_u32 v5, v2, v3
	v_sub_u32_e32 v5, v4, v5
	v_add_u32_e32 v6, 1, v2
	v_cmp_ge_u32_e32 vcc, v5, v3
	v_add_u32_e32 v4, 1, v4
	s_nop 0
	v_cndmask_b32_e32 v2, v2, v6, vcc
	v_sub_u32_e32 v6, v5, v3
	v_cndmask_b32_e32 v5, v5, v6, vcc
	v_add_u32_e32 v6, 1, v2
	v_cmp_ge_u32_e32 vcc, v5, v3
	s_nop 1
	v_cndmask_b32_e32 v2, v2, v6, vcc
	v_mul_lo_u32 v5, v3, v2
	v_add_u32_e32 v3, v5, v3
	v_cmp_ne_u32_e32 vcc, v4, v3
	s_and_saveexec_b64 s[6:7], vcc
	s_xor_b64 s[6:7], exec, s[6:7]
	s_cbranch_execz .LBB0_1276
	s_waitcnt lgkmcnt(0)
	v_add_u32_e32 v19, 1, v2
	v_mul_lo_u32 v19, v19, v1
	v_mov_b32_e32 v1, 0x7000
	global_load_dword v1, v1, s[90:91] offset:1024 sc1
	s_add_u32 s12, s90, 0x7400
	s_addc_u32 s13, s91, 0
	s_waitcnt vmcnt(0)
	v_cmp_lt_u32_e32 vcc, v1, v19
	s_and_saveexec_b64 s[8:9], vcc
	s_cbranch_execz .LBB0_1275
	s_add_u32 s10, s90, 0x4200
	s_addc_u32 s11, s91, 0
	s_mov_b32 s3, 1
	s_mov_b64 s[14:15], 0
	v_mov_b32_e32 v1, 0
	s_branch .LBB0_1266

; __device__ __forceinline__ unsigned xb_ld(unsigned* p)              { return __hip_atomic_load(p, __ATOMIC_RELAXED, __HIP_MEMORY_SCOPE_AGENT); }
; __device__ __forceinline__ unsigned xb_add(unsigned* p, unsigned v) { return __hip_atomic_fetch_add(p, v, __ATOMIC_RELAXED, __HIP_MEMORY_SCOPE_AGENT); }
; #define XB_SPIN(cond, bar) do { unsigned _sp = 0; while (cond) { __builtin_amdgcn_s_sleep(1); \
;     if ((++_sp & 255u) == 0u) { if (xb_ld(&(bar)[XB_TMO])) break; if (_sp > XB_SPIN_CAP) { atomicAdd(&(bar)[XB_TMO], 1u); break; } } } } while (0)
; __device__ __forceinline__ void xcd_barrier(const XcdBarrier& b) {
;     ...
;             if (og + 1u == (tg + 1u) * nx) xb_add(&bar[XB_TOPGEN], 1u);
;             else XB_SPIN(xb_ld(&bar[XB_TOPGEN]) == tg, bar);
;             __builtin_amdgcn_fence(__ATOMIC_ACQUIRE, "agent");
;             xb_add(&bar[XB_XGEN(b.x)], 1u);
;             asm volatile("s_waitcnt vmcnt(0)" ::: "memory");
;         } else {
;             XB_SPIN(xb_ld(&bar[XB_XGEN(b.x)]) == gen, bar);
;             __builtin_amdgcn_fence(__ATOMIC_ACQUIRE, "agent");
;             asm volatile("s_waitcnt vmcnt(0)" ::: "memory");
.LBB0_1291:
	s_or_b64 exec, exec, s[6:7]
	s_and_saveexec_b64 s[6:7], s[10:11]
	s_cbranch_execz .LBB0_1293
	v_mov_b32_e32 v1, 1
.LBB0_1293:
	s_or_b64 exec, exec, s[6:7]
	v_mov_b32_e32 v1, 0x2000
	v_mov_b32_e32 v2, 1
	s_waitcnt vmcnt(0)
	buffer_inv sc1
	s_waitcnt vmcnt(0)

; __device__ __forceinline__ unsigned xb_ld(unsigned* p)              { return __hip_atomic_load(p, __ATOMIC_RELAXED, __HIP_MEMORY_SCOPE_AGENT); }
; __device__ __forceinline__ unsigned xb_add(unsigned* p, unsigned v) { return __hip_atomic_fetch_add(p, v, __ATOMIC_RELAXED, __HIP_MEMORY_SCOPE_AGENT); }
; #define XB_SPIN(cond, bar) do { unsigned _sp = 0; while (cond) { __builtin_amdgcn_s_sleep(1); \
;     if ((++_sp & 255u) == 0u) { if (xb_ld(&(bar)[XB_TMO])) break; if (_sp > XB_SPIN_CAP) { atomicAdd(&(bar)[XB_TMO], 1u); break; } } } } while (0)
; __device__ __forceinline__ void xcd_barrier(const XcdBarrier& b) {
;     ...
;             if (og + 1u == (tg + 1u) * nx) xb_add(&bar[XB_TOPGEN], 1u);
;             else XB_SPIN(xb_ld(&bar[XB_TOPGEN]) == tg, bar);
;             __builtin_amdgcn_fence(__ATOMIC_ACQUIRE, "agent");
;             xb_add(&bar[XB_XGEN(b.x)], 1u);
;             asm volatile("s_waitcnt vmcnt(0)" ::: "memory");
;         } else {
;             XB_SPIN(xb_ld(&bar[XB_XGEN(b.x)]) == gen, bar);
;             __builtin_amdgcn_fence(__ATOMIC_ACQUIRE, "agent");
;             asm volatile("s_waitcnt vmcnt(0)" ::: "memory");
.LBB0_1351:
	s_or_b64 exec, exec, s[6:7]
	s_and_saveexec_b64 s[6:7], s[10:11]
	s_cbranch_execz .LBB0_1353
	v_mov_b32_e32 v1, 1
.LBB0_1353:
	s_or_b64 exec, exec, s[6:7]
	v_mov_b32_e32 v1, 0x2000
	v_mov_b32_e32 v2, 1
	s_waitcnt vmcnt(0)
	buffer_inv sc1
	s_waitcnt vmcnt(0)

; __device__ __forceinline__ unsigned xb_ld(unsigned* p)              { return __hip_atomic_load(p, __ATOMIC_RELAXED, __HIP_MEMORY_SCOPE_AGENT); }
; __device__ __forceinline__ unsigned xb_add(unsigned* p, unsigned v) { return __hip_atomic_fetch_add(p, v, __ATOMIC_RELAXED, __HIP_MEMORY_SCOPE_AGENT); }
; #define XB_SPIN(cond, bar) do { unsigned _sp = 0; while (cond) { __builtin_amdgcn_s_sleep(1); \
;     if ((++_sp & 255u) == 0u) { if (xb_ld(&(bar)[XB_TMO])) break; if (_sp > XB_SPIN_CAP) { atomicAdd(&(bar)[XB_TMO], 1u); break; } } } } while (0)
; __device__ __forceinline__ void xcd_barrier(const XcdBarrier& b) {
;     ...
;             if (og + 1u == (tg + 1u) * nx) xb_add(&bar[XB_TOPGEN], 1u);
;             else XB_SPIN(xb_ld(&bar[XB_TOPGEN]) == tg, bar);
;             __builtin_amdgcn_fence(__ATOMIC_ACQUIRE, "agent");
;             xb_add(&bar[XB_XGEN(b.x)], 1u);
;             asm volatile("s_waitcnt vmcnt(0)" ::: "memory");
;         } else {
;             XB_SPIN(xb_ld(&bar[XB_XGEN(b.x)]) == gen, bar);
;             __builtin_amdgcn_fence(__ATOMIC_ACQUIRE, "agent");
;             asm volatile("s_waitcnt vmcnt(0)" ::: "memory");
.LBB0_1433:
	s_or_b64 exec, exec, s[6:7]
	s_and_saveexec_b64 s[6:7], s[10:11]
	s_cbranch_execz .LBB0_1435
	v_mov_b32_e32 v1, 1
.LBB0_1435:
	s_or_b64 exec, exec, s[6:7]
	v_mov_b32_e32 v1, 0x2000
	v_mov_b32_e32 v2, 1
	s_waitcnt vmcnt(0)
	buffer_inv sc1
	s_waitcnt vmcnt(0)

; __device__ __forceinline__ unsigned xb_ld(unsigned* p)              { return __hip_atomic_load(p, __ATOMIC_RELAXED, __HIP_MEMORY_SCOPE_AGENT); }
; __device__ __forceinline__ unsigned xb_add(unsigned* p, unsigned v) { return __hip_atomic_fetch_add(p, v, __ATOMIC_RELAXED, __HIP_MEMORY_SCOPE_AGENT); }
; #define XB_SPIN(cond, bar) do { unsigned _sp = 0; while (cond) { __builtin_amdgcn_s_sleep(1); \
;     if ((++_sp & 255u) == 0u) { if (xb_ld(&(bar)[XB_TMO])) break; if (_sp > XB_SPIN_CAP) { atomicAdd(&(bar)[XB_TMO], 1u); break; } } } } while (0)
; __device__ __forceinline__ void xcd_barrier(const XcdBarrier& b) {
;     ...
;             if (og + 1u == (tg + 1u) * nx) xb_add(&bar[XB_TOPGEN], 1u);
;             else XB_SPIN(xb_ld(&bar[XB_TOPGEN]) == tg, bar);
;             __builtin_amdgcn_fence(__ATOMIC_ACQUIRE, "agent");
;             xb_add(&bar[XB_XGEN(b.x)], 1u);
;             asm volatile("s_waitcnt vmcnt(0)" ::: "memory");
;         } else {
;             XB_SPIN(xb_ld(&bar[XB_XGEN(b.x)]) == gen, bar);
;             __builtin_amdgcn_fence(__ATOMIC_ACQUIRE, "agent");
;             asm volatile("s_waitcnt vmcnt(0)" ::: "memory");
.LBB0_1546:
	s_or_b64 exec, exec, s[6:7]
	s_and_saveexec_b64 s[6:7], s[10:11]
	s_cbranch_execz .LBB0_1548
	v_mov_b32_e32 v1, 1
.LBB0_1548:
	s_or_b64 exec, exec, s[6:7]
	v_mov_b32_e32 v1, 0x2000
	v_mov_b32_e32 v2, 1
	s_waitcnt vmcnt(0)
	buffer_inv sc1
	s_waitcnt vmcnt(0)

; __device__ __forceinline__ unsigned xb_ld(unsigned* p)              { return __hip_atomic_load(p, __ATOMIC_RELAXED, __HIP_MEMORY_SCOPE_AGENT); }
; __device__ __forceinline__ unsigned xb_add(unsigned* p, unsigned v) { return __hip_atomic_fetch_add(p, v, __ATOMIC_RELAXED, __HIP_MEMORY_SCOPE_AGENT); }
; #define XB_SPIN(cond, bar) do { unsigned _sp = 0; while (cond) { __builtin_amdgcn_s_sleep(1); \
;     if ((++_sp & 255u) == 0u) { if (xb_ld(&(bar)[XB_TMO])) break; if (_sp > XB_SPIN_CAP) { atomicAdd(&(bar)[XB_TMO], 1u); break; } } } } while (0)
; __device__ __forceinline__ void xcd_barrier(const XcdBarrier& b) {
;     ...
;             if (og + 1u == (tg + 1u) * nx) xb_add(&bar[XB_TOPGEN], 1u);
;             else XB_SPIN(xb_ld(&bar[XB_TOPGEN]) == tg, bar);
;             __builtin_amdgcn_fence(__ATOMIC_ACQUIRE, "agent");
;             xb_add(&bar[XB_XGEN(b.x)], 1u);
;             asm volatile("s_waitcnt vmcnt(0)" ::: "memory");
;         } else {
;             XB_SPIN(xb_ld(&bar[XB_XGEN(b.x)]) == gen, bar);
;             __builtin_amdgcn_fence(__ATOMIC_ACQUIRE, "agent");
;             asm volatile("s_waitcnt vmcnt(0)" ::: "memory");
.LBB0_1626:
	s_or_b64 exec, exec, s[6:7]
	s_and_saveexec_b64 s[6:7], s[10:11]
	s_cbranch_execz .LBB0_1628
	v_mov_b32_e32 v1, 1
.LBB0_1628:
	s_or_b64 exec, exec, s[6:7]
	v_mov_b32_e32 v1, 0x2000
	v_mov_b32_e32 v2, 1
	s_waitcnt vmcnt(0)
	buffer_inv sc1
	s_waitcnt vmcnt(0)

; __device__ __forceinline__ unsigned xb_ld(unsigned* p)              { return __hip_atomic_load(p, __ATOMIC_RELAXED, __HIP_MEMORY_SCOPE_AGENT); }
; #define XB_SPIN(cond, bar) do { unsigned _sp = 0; while (cond) { __builtin_amdgcn_s_sleep(1); \
;     if ((++_sp & 255u) == 0u) { if (xb_ld(&(bar)[XB_TMO])) break; if (_sp > XB_SPIN_CAP) { atomicAdd(&(bar)[XB_TMO], 1u); break; } } } } while (0)
; __device__ __forceinline__ void xcd_barrier(const XcdBarrier& b) {
;     ...
;             else XB_SPIN(xb_ld(&bar[XB_TOPGEN]) == tg, bar);
.LBB0_1682:
	global_load_dword v2, v1, s[8:9] sc1
	s_add_i32 s3, s3, 1
	s_mov_b64 s[18:19], -1
	s_waitcnt vmcnt(0)
	v_cmp_ge_u32_e32 vcc, v2, v19
	s_orn2_b64 s[22:23], vcc, exec
	s_branch .LBB0_1677

; __device__ __forceinline__ unsigned xb_ld(unsigned* p)              { return __hip_atomic_load(p, __ATOMIC_RELAXED, __HIP_MEMORY_SCOPE_AGENT); }
; __device__ __forceinline__ unsigned xb_add(unsigned* p, unsigned v) { return __hip_atomic_fetch_add(p, v, __ATOMIC_RELAXED, __HIP_MEMORY_SCOPE_AGENT); }
; #define XB_SPIN(cond, bar) do { unsigned _sp = 0; while (cond) { __builtin_amdgcn_s_sleep(1); \
;     if ((++_sp & 255u) == 0u) { if (xb_ld(&(bar)[XB_TMO])) break; if (_sp > XB_SPIN_CAP) { atomicAdd(&(bar)[XB_TMO], 1u); break; } } } } while (0)
; __device__ __forceinline__ void xcd_barrier(const XcdBarrier& b) {
;     ...
;             if (og + 1u == (tg + 1u) * nx) xb_add(&bar[XB_TOPGEN], 1u);
;             else XB_SPIN(xb_ld(&bar[XB_TOPGEN]) == tg, bar);
;             __builtin_amdgcn_fence(__ATOMIC_ACQUIRE, "agent");
;             xb_add(&bar[XB_XGEN(b.x)], 1u);
;             asm volatile("s_waitcnt vmcnt(0)" ::: "memory");
;         } else {
;             XB_SPIN(xb_ld(&bar[XB_XGEN(b.x)]) == gen, bar);
;             __builtin_amdgcn_fence(__ATOMIC_ACQUIRE, "agent");
;             asm volatile("s_waitcnt vmcnt(0)" ::: "memory");
.LBB0_1686:
	s_or_b64 exec, exec, s[6:7]
	s_and_saveexec_b64 s[6:7], s[10:11]
	s_cbranch_execz .LBB0_1688
	v_mov_b32_e32 v1, 1
.LBB0_1688:
	s_or_b64 exec, exec, s[6:7]
	v_mov_b32_e32 v1, 0x2000
	v_mov_b32_e32 v2, 1
	s_waitcnt vmcnt(0)
	buffer_inv sc1
	s_waitcnt vmcnt(0)

; __device__ __forceinline__ unsigned xb_ld(unsigned* p)              { return __hip_atomic_load(p, __ATOMIC_RELAXED, __HIP_MEMORY_SCOPE_AGENT); }
; __device__ __forceinline__ unsigned xb_add(unsigned* p, unsigned v) { return __hip_atomic_fetch_add(p, v, __ATOMIC_RELAXED, __HIP_MEMORY_SCOPE_AGENT); }
; #define XB_SPIN(cond, bar) do { unsigned _sp = 0; while (cond) { __builtin_amdgcn_s_sleep(1); \
;     if ((++_sp & 255u) == 0u) { if (xb_ld(&(bar)[XB_TMO])) break; if (_sp > XB_SPIN_CAP) { atomicAdd(&(bar)[XB_TMO], 1u); break; } } } } while (0)
; __device__ __forceinline__ void xcd_barrier(const XcdBarrier& b) {
;     ...
;             if (og + 1u == (tg + 1u) * nx) xb_add(&bar[XB_TOPGEN], 1u);
;             else XB_SPIN(xb_ld(&bar[XB_TOPGEN]) == tg, bar);
;             __builtin_amdgcn_fence(__ATOMIC_ACQUIRE, "agent");
;             xb_add(&bar[XB_XGEN(b.x)], 1u);
;             asm volatile("s_waitcnt vmcnt(0)" ::: "memory");
;         } else {
;             XB_SPIN(xb_ld(&bar[XB_XGEN(b.x)]) == gen, bar);
;             __builtin_amdgcn_fence(__ATOMIC_ACQUIRE, "agent");
;             asm volatile("s_waitcnt vmcnt(0)" ::: "memory");
.LBB0_1768:
	s_or_b64 exec, exec, s[6:7]
	s_and_saveexec_b64 s[6:7], s[10:11]
	s_cbranch_execz .LBB0_1770
	v_mov_b32_e32 v1, 1
.LBB0_1770:
	s_or_b64 exec, exec, s[6:7]
	v_mov_b32_e32 v1, 0x2000
	v_mov_b32_e32 v2, 1
	s_waitcnt vmcnt(0)
	buffer_inv sc1
	s_waitcnt vmcnt(0)

; __device__ __forceinline__ unsigned xb_ld(unsigned* p)              { return __hip_atomic_load(p, __ATOMIC_RELAXED, __HIP_MEMORY_SCOPE_AGENT); }
; __device__ __forceinline__ unsigned xb_add(unsigned* p, unsigned v) { return __hip_atomic_fetch_add(p, v, __ATOMIC_RELAXED, __HIP_MEMORY_SCOPE_AGENT); }
; #define XB_SPIN(cond, bar) do { unsigned _sp = 0; while (cond) { __builtin_amdgcn_s_sleep(1); \
;     if ((++_sp & 255u) == 0u) { if (xb_ld(&(bar)[XB_TMO])) break; if (_sp > XB_SPIN_CAP) { atomicAdd(&(bar)[XB_TMO], 1u); break; } } } } while (0)
; __device__ __forceinline__ void xcd_barrier(const XcdBarrier& b) {
;     ...
;             if (og + 1u == (tg + 1u) * nx) xb_add(&bar[XB_TOPGEN], 1u);
;             else XB_SPIN(xb_ld(&bar[XB_TOPGEN]) == tg, bar);
;             __builtin_amdgcn_fence(__ATOMIC_ACQUIRE, "agent");
;             xb_add(&bar[XB_XGEN(b.x)], 1u);
;             asm volatile("s_waitcnt vmcnt(0)" ::: "memory");
;         } else {
;             XB_SPIN(xb_ld(&bar[XB_XGEN(b.x)]) == gen, bar);
;             __builtin_amdgcn_fence(__ATOMIC_ACQUIRE, "agent");
;             asm volatile("s_waitcnt vmcnt(0)" ::: "memory");
.LBB0_1832:
	s_or_b64 exec, exec, s[6:7]
	s_and_saveexec_b64 s[6:7], s[10:11]
	s_cbranch_execz .LBB0_1834
	v_mov_b32_e32 v1, 1
.LBB0_1834:
	s_or_b64 exec, exec, s[6:7]
	v_mov_b32_e32 v1, 0x2000
	v_mov_b32_e32 v2, 1
	s_waitcnt vmcnt(0)
	buffer_inv sc1
	s_waitcnt vmcnt(0)

; __device__ __forceinline__ unsigned xb_ld(unsigned* p)              { return __hip_atomic_load(p, __ATOMIC_RELAXED, __HIP_MEMORY_SCOPE_AGENT); }
; __device__ __forceinline__ unsigned xb_add(unsigned* p, unsigned v) { return __hip_atomic_fetch_add(p, v, __ATOMIC_RELAXED, __HIP_MEMORY_SCOPE_AGENT); }
; #define XB_SPIN(cond, bar) do { unsigned _sp = 0; while (cond) { __builtin_amdgcn_s_sleep(1); \
;     if ((++_sp & 255u) == 0u) { if (xb_ld(&(bar)[XB_TMO])) break; if (_sp > XB_SPIN_CAP) { atomicAdd(&(bar)[XB_TMO], 1u); break; } } } } while (0)
; __device__ __forceinline__ void xcd_barrier(const XcdBarrier& b) {
;     ...
;             if (og + 1u == (tg + 1u) * nx) xb_add(&bar[XB_TOPGEN], 1u);
;             else XB_SPIN(xb_ld(&bar[XB_TOPGEN]) == tg, bar);
;             __builtin_amdgcn_fence(__ATOMIC_ACQUIRE, "agent");
;             xb_add(&bar[XB_XGEN(b.x)], 1u);
;             asm volatile("s_waitcnt vmcnt(0)" ::: "memory");
;         } else {
;             XB_SPIN(xb_ld(&bar[XB_XGEN(b.x)]) == gen, bar);
;             __builtin_amdgcn_fence(__ATOMIC_ACQUIRE, "agent");
;             asm volatile("s_waitcnt vmcnt(0)" ::: "memory");
.LBB0_1907:
	s_or_b64 exec, exec, s[6:7]
	s_and_saveexec_b64 s[6:7], s[10:11]
	s_cbranch_execz .LBB0_1909
	v_mov_b32_e32 v1, 1
.LBB0_1909:
	s_or_b64 exec, exec, s[6:7]
	v_mov_b32_e32 v1, 0x2000
	v_mov_b32_e32 v2, 1
	s_waitcnt vmcnt(0)
	buffer_inv sc1
	s_waitcnt vmcnt(0)

; __device__ __forceinline__ unsigned xb_ld(unsigned* p)              { return __hip_atomic_load(p, __ATOMIC_RELAXED, __HIP_MEMORY_SCOPE_AGENT); }
; #define XB_SPIN(cond, bar) do { unsigned _sp = 0; while (cond) { __builtin_amdgcn_s_sleep(1); \
;     if ((++_sp & 255u) == 0u) { if (xb_ld(&(bar)[XB_TMO])) break; if (_sp > XB_SPIN_CAP) { atomicAdd(&(bar)[XB_TMO], 1u); break; } } } } while (0)
; __device__ __forceinline__ void xcd_barrier(const XcdBarrier& b) {
;     ...
;             XB_SPIN(xb_ld(&bar[XB_XGEN(b.x)]) == gen, bar);
.LBB0_1949:
	global_load_dword v3, v1, s[16:17] sc1
	s_add_i32 s3, s3, 1
	s_mov_b64 s[28:29], -1
	s_waitcnt vmcnt(0)
	v_cmp_ge_u32_e32 vcc, v3, v19
	s_orn2_b64 s[22:23], vcc, exec
	s_branch .LBB0_1944

; __device__ __forceinline__ unsigned xb_ld(unsigned* p)              { return __hip_atomic_load(p, __ATOMIC_RELAXED, __HIP_MEMORY_SCOPE_AGENT); }
; #define XB_SPIN(cond, bar) do { unsigned _sp = 0; while (cond) { __builtin_amdgcn_s_sleep(1); \
;     if ((++_sp & 255u) == 0u) { if (xb_ld(&(bar)[XB_TMO])) break; if (_sp > XB_SPIN_CAP) { atomicAdd(&(bar)[XB_TMO], 1u); break; } } } } while (0)
; __device__ __forceinline__ void xcd_barrier(const XcdBarrier& b) {
;     ...
;             else XB_SPIN(xb_ld(&bar[XB_TOPGEN]) == tg, bar);
.LBB0_1966:
	global_load_dword v2, v1, s[12:13] sc1
	s_add_i32 s3, s3, 1
	s_mov_b64 s[22:23], -1
	s_waitcnt vmcnt(0)
	v_cmp_ge_u32_e32 vcc, v2, v19
	s_orn2_b64 s[30:31], vcc, exec
	s_branch .LBB0_1961

; __device__ __forceinline__ unsigned xb_ld(unsigned* p)              { return __hip_atomic_load(p, __ATOMIC_RELAXED, __HIP_MEMORY_SCOPE_AGENT); }
; __device__ __forceinline__ unsigned xb_add(unsigned* p, unsigned v) { return __hip_atomic_fetch_add(p, v, __ATOMIC_RELAXED, __HIP_MEMORY_SCOPE_AGENT); }
; #define XB_SPIN(cond, bar) do { unsigned _sp = 0; while (cond) { __builtin_amdgcn_s_sleep(1); \
;     if ((++_sp & 255u) == 0u) { if (xb_ld(&(bar)[XB_TMO])) break; if (_sp > XB_SPIN_CAP) { atomicAdd(&(bar)[XB_TMO], 1u); break; } } } } while (0)
; __device__ __forceinline__ void xcd_barrier(const XcdBarrier& b) {
;     ...
;             if (og + 1u == (tg + 1u) * nx) xb_add(&bar[XB_TOPGEN], 1u);
;             else XB_SPIN(xb_ld(&bar[XB_TOPGEN]) == tg, bar);
;             __builtin_amdgcn_fence(__ATOMIC_ACQUIRE, "agent");
;             xb_add(&bar[XB_XGEN(b.x)], 1u);
;             asm volatile("s_waitcnt vmcnt(0)" ::: "memory");
;         } else {
;             XB_SPIN(xb_ld(&bar[XB_XGEN(b.x)]) == gen, bar);
;             __builtin_amdgcn_fence(__ATOMIC_ACQUIRE, "agent");
;             asm volatile("s_waitcnt vmcnt(0)" ::: "memory");
.LBB0_1970:
	s_or_b64 exec, exec, s[10:11]
	s_and_saveexec_b64 s[10:11], s[14:15]
	s_cbranch_execz .LBB0_1972
	v_mov_b32_e32 v1, 1
.LBB0_1972:
	s_or_b64 exec, exec, s[10:11]
	v_mov_b32_e32 v1, 0x2000
	v_mov_b32_e32 v2, 1
	s_waitcnt vmcnt(0)
	buffer_inv sc1
	s_waitcnt vmcnt(0)

; __device__ __forceinline__ unsigned xb_ld(unsigned* p)              { return __hip_atomic_load(p, __ATOMIC_RELAXED, __HIP_MEMORY_SCOPE_AGENT); }
; __device__ __forceinline__ unsigned xb_add(unsigned* p, unsigned v) { return __hip_atomic_fetch_add(p, v, __ATOMIC_RELAXED, __HIP_MEMORY_SCOPE_AGENT); }
; #define XB_SPIN(cond, bar) do { unsigned _sp = 0; while (cond) { __builtin_amdgcn_s_sleep(1); \
;     if ((++_sp & 255u) == 0u) { if (xb_ld(&(bar)[XB_TMO])) break; if (_sp > XB_SPIN_CAP) { atomicAdd(&(bar)[XB_TMO], 1u); break; } } } } while (0)
; __device__ __forceinline__ void xcd_barrier(const XcdBarrier& b) {
;     ...
;             if (og + 1u == (tg + 1u) * nx) xb_add(&bar[XB_TOPGEN], 1u);
;             else XB_SPIN(xb_ld(&bar[XB_TOPGEN]) == tg, bar);
;             __builtin_amdgcn_fence(__ATOMIC_ACQUIRE, "agent");
;             xb_add(&bar[XB_XGEN(b.x)], 1u);
;             asm volatile("s_waitcnt vmcnt(0)" ::: "memory");
;         } else {
;             XB_SPIN(xb_ld(&bar[XB_XGEN(b.x)]) == gen, bar);
;             __builtin_amdgcn_fence(__ATOMIC_ACQUIRE, "agent");
;             asm volatile("s_waitcnt vmcnt(0)" ::: "memory");
.LBB0_2036:
	s_or_b64 exec, exec, s[6:7]
	s_and_saveexec_b64 s[6:7], s[10:11]
	s_cbranch_execz .LBB0_2038
	v_mov_b32_e32 v1, 1
.LBB0_2038:
	s_or_b64 exec, exec, s[6:7]
	v_mov_b32_e32 v1, 0x2000
	v_mov_b32_e32 v2, 1
	s_waitcnt vmcnt(0)
	buffer_inv sc1
	s_waitcnt vmcnt(0)
